# v74 + barrier release from TOP counter + rotary in-proj epilogue de-serialised (table loads 2-4 blocks ahead)
# speedup vs baseline: 1.0049x; 1.0049x over previous
; __device__ __forceinline__ unsigned cvt_pk_bf16(float lo, float hi) { unsigned r; asm volatile("v_cvt_pk_bf16_f32 %0, %1, %2" : "=v"(r) : "v"(lo), "v"(hi)); return r; }
;     __device__ __forceinline__ void operator()(const f32x4 (&acc)[2][2][4][2], const Unit& u, int wr, int wc, int fr, int fq) const {
;     ...
;         } else if (u.pn < rot_tiles) {
;             const float sc = u.pn >= 8 ? 0.0625f : 1.0f; const int j0 = wc * 32 + 8 * fq;
; #pragma unroll
;             for (int ai = 0; ai < 2; ++ai)
; #pragma unroll
;                 for (int m = 0; m < 4; ++m) { const int row = row0 + ai * HALF + m * 16; bf16_t* rowp = O + (size_t)row * ldc + col0;
;                     const f32x4 c0 = *(const f32x4*)(ct + (size_t)row * 128 + j0), c1 = *(const f32x4*)(ct + (size_t)row * 128 + j0 + 4);
;                     const f32x4 s0 = *(const f32x4*)(st + (size_t)row * 128 + j0), s1 = *(const f32x4*)(st + (size_t)row * 128 + j0 + 4);
;                     const f32x4 a0 = acc[ai][0][m][0], a1 = acc[ai][0][m][1], b0 = acc[ai][1][m][0], b1 = acc[ai][1][m][1];
;                     const f32x4 p0 = (a0 * c0 - b0 * s0) * sc, p1 = (a1 * c1 - b1 * s1) * sc, q0 = (a0 * s0 + b0 * c0) * sc, q1 = (a1 * s1 + b1 * c1) * sc;
;                     u32x4 w; w.x = cvt_pk_bf16(p0[0], p0[1]); w.y = cvt_pk_bf16(p0[2], p0[3]); w.z = cvt_pk_bf16(p1[0], p1[1]); w.w = cvt_pk_bf16(p1[2], p1[3]);
;                     *(u32x4*)rowp = w;
;                     w.x = cvt_pk_bf16(q0[0], q0[1]); w.y = cvt_pk_bf16(q0[2], q0[3]); w.z = cvt_pk_bf16(q1[0], q1[1]); w.w = cvt_pk_bf16(q1[2], q1[3]);
;                     *(u32x4*)(rowp + HALF) = w; }
.LBB0_400:
	s_and_b64 vcc, exec, s[0:1]
	s_cbranch_vccz .LBB0_402
	v_ashrrev_i32_e32 v151, 31, v150
	v_mad_i64_i32 v[130:131], s[0:1], v150, s7, 0
	v_lshlrev_b64 v[138:139], 9, v[150:151]
	v_lshl_add_u64 v[130:131], v[130:131], 1, s[56:57]
	v_lshl_add_u64 v[222:223], v[146:147], 0, v[138:139]
	v_lshl_add_u64 v[224:225], v[148:149], 0, v[138:139]
	v_lshl_add_u64 v[164:165], v[130:131], 0, v[0:1]
	s_mov_b32 s12, 0x2000
	s_mov_b32 s13, 0
	s_mov_b32 s14, 0xa000
	s_mov_b32 s15, 0
	s_lshl_b32 s8, s7, 5
	s_mov_b32 s9, 0
	s_mul_i32 s38, s7, 160
	s_mov_b32 s39, 0
	global_load_dwordx4 v[130:133], v[222:223], off offset:16
	global_load_dwordx4 v[134:137], v[222:223], off
	global_load_dwordx4 v[138:141], v[224:225], off offset:16
	global_load_dwordx4 v[172:175], v[224:225], off
	v_lshl_add_u64 v[222:223], v[222:223], 0, s[12:13]
	v_lshl_add_u64 v[224:225], v[224:225], 0, s[12:13]
	global_load_dwordx4 v[206:209], v[222:223], off offset:16
	global_load_dwordx4 v[210:213], v[222:223], off
	global_load_dwordx4 v[214:217], v[224:225], off offset:16
	global_load_dwordx4 v[218:221], v[224:225], off
	v_lshl_add_u64 v[222:223], v[222:223], 0, s[12:13]
	v_lshl_add_u64 v[224:225], v[224:225], 0, s[12:13]
	s_cmp_gt_i32 s3, 7
	s_cselect_b64 vcc, -1, 0
	v_cndmask_b32_e32 v152, 1.0, v196, vcc
	s_waitcnt vmcnt(4)
	v_pk_mul_f32 v[182:183], v[110:111], v[138:139]
	v_pk_mul_f32 v[178:179], v[126:127], v[172:173]
	v_pk_mul_f32 v[138:139], v[102:103], v[138:139]
	v_pk_mul_f32 v[176:177], v[128:129], v[174:175]
	v_pk_fma_f32 v[178:179], v[118:119], v[134:135], v[178:179] neg_lo:[0,0,1] neg_hi:[0,0,1]
	v_pk_mul_f32 v[180:181], v[112:113], v[140:141]
	v_pk_fma_f32 v[182:183], v[102:103], v[130:131], v[182:183] neg_lo:[0,0,1] neg_hi:[0,0,1]
	v_pk_mul_f32 v[172:173], v[118:119], v[172:173]
	v_pk_mul_f32 v[140:141], v[104:105], v[140:141]
	v_pk_fma_f32 v[130:131], v[110:111], v[130:131], v[138:139]
	v_pk_fma_f32 v[176:177], v[120:121], v[136:137], v[176:177] neg_lo:[0,0,1] neg_hi:[0,0,1]
	v_pk_mul_f32 v[178:179], v[152:153], v[178:179] op_sel_hi:[0,1]
	v_pk_fma_f32 v[180:181], v[104:105], v[132:133], v[180:181] neg_lo:[0,0,1] neg_hi:[0,0,1]
	v_pk_mul_f32 v[174:175], v[120:121], v[174:175]
	v_pk_fma_f32 v[134:135], v[126:127], v[134:135], v[172:173]
	v_pk_fma_f32 v[132:133], v[112:113], v[132:133], v[140:141]
	v_pk_mul_f32 v[140:141], v[152:153], v[130:131] op_sel_hi:[0,1]
	v_cvt_pk_bf16_f32 v130, v178, v179
	v_pk_mul_f32 v[176:177], v[152:153], v[176:177] op_sel_hi:[0,1]
	v_pk_mul_f32 v[180:181], v[152:153], v[180:181] op_sel_hi:[0,1]
	v_pk_mul_f32 v[182:183], v[152:153], v[182:183] op_sel_hi:[0,1]
	v_pk_fma_f32 v[136:137], v[128:129], v[136:137], v[174:175]
	v_pk_mul_f32 v[134:135], v[152:153], v[134:135] op_sel_hi:[0,1]
	v_pk_mul_f32 v[138:139], v[152:153], v[132:133] op_sel_hi:[0,1]
	v_cvt_pk_bf16_f32 v131, v176, v177
	v_cvt_pk_bf16_f32 v132, v182, v183
	v_cvt_pk_bf16_f32 v133, v180, v181
	global_store_dwordx4 v[164:165], v[130:133], off
	v_pk_mul_f32 v[136:137], v[152:153], v[136:137] op_sel_hi:[0,1]
	s_nop 0
	v_cvt_pk_bf16_f32 v130, v134, v135
	v_cvt_pk_bf16_f32 v131, v136, v137
	v_cvt_pk_bf16_f32 v132, v140, v141
	v_cvt_pk_bf16_f32 v133, v138, v139
	global_store_dwordx4 v[164:165], v[130:133], off offset:256
	s_nop 1
	v_lshl_add_u64 v[164:165], v[164:165], 0, s[8:9]
	global_load_dwordx4 v[102:105], v[222:223], off offset:16
	global_load_dwordx4 v[110:113], v[222:223], off
	global_load_dwordx4 v[118:121], v[224:225], off offset:16
	global_load_dwordx4 v[126:129], v[224:225], off
	v_lshl_add_u64 v[222:223], v[222:223], 0, s[12:13]
	v_lshl_add_u64 v[224:225], v[224:225], 0, s[12:13]
	global_load_dwordx4 v[130:133], v[222:223], off offset:16
	global_load_dwordx4 v[134:137], v[222:223], off
	global_load_dwordx4 v[138:141], v[224:225], off offset:16
	global_load_dwordx4 v[172:175], v[224:225], off
	v_lshl_add_u64 v[222:223], v[222:223], 0, s[14:15]
	v_lshl_add_u64 v[224:225], v[224:225], 0, s[14:15]
	s_waitcnt vmcnt(10)
	v_pk_mul_f32 v[182:183], v[106:107], v[214:215]
	v_pk_mul_f32 v[178:179], v[122:123], v[218:219]
	v_pk_mul_f32 v[214:215], v[98:99], v[214:215]
	v_pk_mul_f32 v[176:177], v[124:125], v[220:221]
	v_pk_fma_f32 v[178:179], v[114:115], v[210:211], v[178:179] neg_lo:[0,0,1] neg_hi:[0,0,1]
	v_pk_mul_f32 v[180:181], v[108:109], v[216:217]
	v_pk_fma_f32 v[182:183], v[98:99], v[206:207], v[182:183] neg_lo:[0,0,1] neg_hi:[0,0,1]
	v_pk_mul_f32 v[218:219], v[114:115], v[218:219]
	v_pk_mul_f32 v[216:217], v[100:101], v[216:217]
	v_pk_fma_f32 v[206:207], v[106:107], v[206:207], v[214:215]
	v_pk_fma_f32 v[176:177], v[116:117], v[212:213], v[176:177] neg_lo:[0,0,1] neg_hi:[0,0,1]
	v_pk_mul_f32 v[178:179], v[152:153], v[178:179] op_sel_hi:[0,1]
	v_pk_fma_f32 v[180:181], v[100:101], v[208:209], v[180:181] neg_lo:[0,0,1] neg_hi:[0,0,1]
	v_pk_mul_f32 v[220:221], v[116:117], v[220:221]
	v_pk_fma_f32 v[210:211], v[122:123], v[210:211], v[218:219]
	v_pk_fma_f32 v[208:209], v[108:109], v[208:209], v[216:217]
	v_pk_mul_f32 v[216:217], v[152:153], v[206:207] op_sel_hi:[0,1]
	v_cvt_pk_bf16_f32 v206, v178, v179
	v_pk_mul_f32 v[176:177], v[152:153], v[176:177] op_sel_hi:[0,1]
	v_pk_mul_f32 v[180:181], v[152:153], v[180:181] op_sel_hi:[0,1]
	v_pk_mul_f32 v[182:183], v[152:153], v[182:183] op_sel_hi:[0,1]
	v_pk_fma_f32 v[212:213], v[124:125], v[212:213], v[220:221]
	v_pk_mul_f32 v[210:211], v[152:153], v[210:211] op_sel_hi:[0,1]
	v_pk_mul_f32 v[214:215], v[152:153], v[208:209] op_sel_hi:[0,1]
	v_cvt_pk_bf16_f32 v207, v176, v177
	v_cvt_pk_bf16_f32 v208, v182, v183
	v_cvt_pk_bf16_f32 v209, v180, v181
	global_store_dwordx4 v[164:165], v[206:209], off
	v_pk_mul_f32 v[212:213], v[152:153], v[212:213] op_sel_hi:[0,1]
	s_nop 0
	v_cvt_pk_bf16_f32 v206, v210, v211
	v_cvt_pk_bf16_f32 v207, v212, v213
	v_cvt_pk_bf16_f32 v208, v216, v217
	v_cvt_pk_bf16_f32 v209, v214, v215
	global_store_dwordx4 v[164:165], v[206:209], off offset:256
	s_nop 1
	v_lshl_add_u64 v[164:165], v[164:165], 0, s[8:9]
	global_load_dwordx4 v[206:209], v[222:223], off offset:16
	global_load_dwordx4 v[210:213], v[222:223], off
	global_load_dwordx4 v[214:217], v[224:225], off offset:16
	global_load_dwordx4 v[218:221], v[224:225], off
	v_lshl_add_u64 v[222:223], v[222:223], 0, s[12:13]
	v_lshl_add_u64 v[224:225], v[224:225], 0, s[12:13]
	global_load_dwordx4 v[98:101], v[222:223], off offset:16
	global_load_dwordx4 v[106:109], v[222:223], off
	global_load_dwordx4 v[114:117], v[224:225], off offset:16
	global_load_dwordx4 v[122:125], v[224:225], off
	v_lshl_add_u64 v[222:223], v[222:223], 0, s[12:13]
	v_lshl_add_u64 v[224:225], v[224:225], 0, s[12:13]
	s_waitcnt vmcnt(14)
; __device__ __forceinline__ unsigned cvt_pk_bf16(float lo, float hi) { unsigned r; asm volatile("v_cvt_pk_bf16_f32 %0, %1, %2" : "=v"(r) : "v"(lo), "v"(hi)); return r; }
;     __device__ __forceinline__ void operator()(const f32x4 (&acc)[2][2][4][2], const Unit& u, int wr, int wc, int fr, int fq) const {
;     ...
;         } else if (u.pn < rot_tiles) {
;             const float sc = u.pn >= 8 ? 0.0625f : 1.0f; const int j0 = wc * 32 + 8 * fq;
; #pragma unroll
;             for (int ai = 0; ai < 2; ++ai)
; #pragma unroll
;                 for (int m = 0; m < 4; ++m) { const int row = row0 + ai * HALF + m * 16; bf16_t* rowp = O + (size_t)row * ldc + col0;
;                     const f32x4 c0 = *(const f32x4*)(ct + (size_t)row * 128 + j0), c1 = *(const f32x4*)(ct + (size_t)row * 128 + j0 + 4);
;                     const f32x4 s0 = *(const f32x4*)(st + (size_t)row * 128 + j0), s1 = *(const f32x4*)(st + (size_t)row * 128 + j0 + 4);
;                     const f32x4 a0 = acc[ai][0][m][0], a1 = acc[ai][0][m][1], b0 = acc[ai][1][m][0], b1 = acc[ai][1][m][1];
;                     const f32x4 p0 = (a0 * c0 - b0 * s0) * sc, p1 = (a1 * c1 - b1 * s1) * sc, q0 = (a0 * s0 + b0 * c0) * sc, q1 = (a1 * s1 + b1 * c1) * sc;
;                     u32x4 w; w.x = cvt_pk_bf16(p0[0], p0[1]); w.y = cvt_pk_bf16(p0[2], p0[3]); w.z = cvt_pk_bf16(p1[0], p1[1]); w.w = cvt_pk_bf16(p1[2], p1[3]);
;                     *(u32x4*)rowp = w;
;                     w.x = cvt_pk_bf16(q0[0], q0[1]); w.y = cvt_pk_bf16(q0[2], q0[3]); w.z = cvt_pk_bf16(q1[0], q1[1]); w.w = cvt_pk_bf16(q1[2], q1[3]);
;                     *(u32x4*)(rowp + HALF) = w; }
	v_pk_mul_f32 v[182:183], v[78:79], v[118:119]
	v_pk_mul_f32 v[178:179], v[94:95], v[126:127]
	v_pk_mul_f32 v[118:119], v[70:71], v[118:119]
	v_pk_mul_f32 v[176:177], v[96:97], v[128:129]
	v_pk_fma_f32 v[178:179], v[86:87], v[110:111], v[178:179] neg_lo:[0,0,1] neg_hi:[0,0,1]
	v_pk_mul_f32 v[180:181], v[80:81], v[120:121]
	v_pk_fma_f32 v[182:183], v[70:71], v[102:103], v[182:183] neg_lo:[0,0,1] neg_hi:[0,0,1]
	v_pk_mul_f32 v[126:127], v[86:87], v[126:127]
	v_pk_mul_f32 v[120:121], v[72:73], v[120:121]
	v_pk_fma_f32 v[102:103], v[78:79], v[102:103], v[118:119]
	v_pk_fma_f32 v[176:177], v[88:89], v[112:113], v[176:177] neg_lo:[0,0,1] neg_hi:[0,0,1]
	v_pk_mul_f32 v[178:179], v[152:153], v[178:179] op_sel_hi:[0,1]
	v_pk_fma_f32 v[180:181], v[72:73], v[104:105], v[180:181] neg_lo:[0,0,1] neg_hi:[0,0,1]
	v_pk_mul_f32 v[128:129], v[88:89], v[128:129]
	v_pk_fma_f32 v[110:111], v[94:95], v[110:111], v[126:127]
	v_pk_fma_f32 v[104:105], v[80:81], v[104:105], v[120:121]
	v_pk_mul_f32 v[120:121], v[152:153], v[102:103] op_sel_hi:[0,1]
	v_cvt_pk_bf16_f32 v102, v178, v179
	v_pk_mul_f32 v[176:177], v[152:153], v[176:177] op_sel_hi:[0,1]
	v_pk_mul_f32 v[180:181], v[152:153], v[180:181] op_sel_hi:[0,1]
	v_pk_mul_f32 v[182:183], v[152:153], v[182:183] op_sel_hi:[0,1]
	v_pk_fma_f32 v[112:113], v[96:97], v[112:113], v[128:129]
	v_pk_mul_f32 v[110:111], v[152:153], v[110:111] op_sel_hi:[0,1]
	v_pk_mul_f32 v[118:119], v[152:153], v[104:105] op_sel_hi:[0,1]
	v_cvt_pk_bf16_f32 v103, v176, v177
	v_cvt_pk_bf16_f32 v104, v182, v183
	v_cvt_pk_bf16_f32 v105, v180, v181
	global_store_dwordx4 v[164:165], v[102:105], off
	v_pk_mul_f32 v[112:113], v[152:153], v[112:113] op_sel_hi:[0,1]
	s_nop 0
	v_cvt_pk_bf16_f32 v102, v110, v111
	v_cvt_pk_bf16_f32 v103, v112, v113
	v_cvt_pk_bf16_f32 v104, v120, v121
	v_cvt_pk_bf16_f32 v105, v118, v119
	global_store_dwordx4 v[164:165], v[102:105], off offset:256
	s_nop 1
	v_lshl_add_u64 v[164:165], v[164:165], 0, s[8:9]
	global_load_dwordx4 v[102:105], v[222:223], off offset:16
	global_load_dwordx4 v[110:113], v[222:223], off
	global_load_dwordx4 v[118:121], v[224:225], off offset:16
	global_load_dwordx4 v[126:129], v[224:225], off
	v_lshl_add_u64 v[222:223], v[222:223], 0, s[12:13]
	v_lshl_add_u64 v[224:225], v[224:225], 0, s[12:13]
	s_waitcnt vmcnt(16)
	v_pk_mul_f32 v[182:183], v[74:75], v[138:139]
	v_pk_mul_f32 v[178:179], v[90:91], v[172:173]
	v_pk_mul_f32 v[138:139], v[66:67], v[138:139]
	v_pk_mul_f32 v[176:177], v[92:93], v[174:175]
	v_pk_fma_f32 v[178:179], v[82:83], v[134:135], v[178:179] neg_lo:[0,0,1] neg_hi:[0,0,1]
	v_pk_mul_f32 v[180:181], v[76:77], v[140:141]
	v_pk_fma_f32 v[182:183], v[66:67], v[130:131], v[182:183] neg_lo:[0,0,1] neg_hi:[0,0,1]
	v_pk_mul_f32 v[172:173], v[82:83], v[172:173]
	v_pk_mul_f32 v[140:141], v[68:69], v[140:141]
	v_pk_fma_f32 v[130:131], v[74:75], v[130:131], v[138:139]
	v_pk_fma_f32 v[176:177], v[84:85], v[136:137], v[176:177] neg_lo:[0,0,1] neg_hi:[0,0,1]
	v_pk_mul_f32 v[178:179], v[152:153], v[178:179] op_sel_hi:[0,1]
	v_pk_fma_f32 v[180:181], v[68:69], v[132:133], v[180:181] neg_lo:[0,0,1] neg_hi:[0,0,1]
	v_pk_mul_f32 v[174:175], v[84:85], v[174:175]
	v_pk_fma_f32 v[134:135], v[90:91], v[134:135], v[172:173]
	v_pk_fma_f32 v[132:133], v[76:77], v[132:133], v[140:141]
	v_pk_mul_f32 v[140:141], v[152:153], v[130:131] op_sel_hi:[0,1]
	v_cvt_pk_bf16_f32 v130, v178, v179
	v_pk_mul_f32 v[176:177], v[152:153], v[176:177] op_sel_hi:[0,1]
	v_pk_mul_f32 v[180:181], v[152:153], v[180:181] op_sel_hi:[0,1]
	v_pk_mul_f32 v[182:183], v[152:153], v[182:183] op_sel_hi:[0,1]
	v_pk_fma_f32 v[136:137], v[92:93], v[136:137], v[174:175]
	v_pk_mul_f32 v[134:135], v[152:153], v[134:135] op_sel_hi:[0,1]
	v_pk_mul_f32 v[138:139], v[152:153], v[132:133] op_sel_hi:[0,1]
	v_cvt_pk_bf16_f32 v131, v176, v177
	v_cvt_pk_bf16_f32 v132, v182, v183
	v_cvt_pk_bf16_f32 v133, v180, v181
	global_store_dwordx4 v[164:165], v[130:133], off
	v_pk_mul_f32 v[136:137], v[152:153], v[136:137] op_sel_hi:[0,1]
	s_nop 0
	v_cvt_pk_bf16_f32 v130, v134, v135
	v_cvt_pk_bf16_f32 v131, v136, v137
	v_cvt_pk_bf16_f32 v132, v140, v141
	v_cvt_pk_bf16_f32 v133, v138, v139
	global_store_dwordx4 v[164:165], v[130:133], off offset:256
	s_nop 1
	v_lshl_add_u64 v[164:165], v[164:165], 0, s[38:39]
	global_load_dwordx4 v[130:133], v[222:223], off offset:16
	global_load_dwordx4 v[134:137], v[222:223], off
	global_load_dwordx4 v[138:141], v[224:225], off offset:16
	global_load_dwordx4 v[172:175], v[224:225], off
	s_waitcnt vmcnt(16)
	v_pk_mul_f32 v[182:183], v[46:47], v[214:215]
	v_pk_mul_f32 v[178:179], v[62:63], v[218:219]
	v_pk_mul_f32 v[214:215], v[38:39], v[214:215]
	v_pk_mul_f32 v[176:177], v[64:65], v[220:221]
	v_pk_fma_f32 v[178:179], v[54:55], v[210:211], v[178:179] neg_lo:[0,0,1] neg_hi:[0,0,1]
	v_pk_mul_f32 v[180:181], v[48:49], v[216:217]
	v_pk_fma_f32 v[182:183], v[38:39], v[206:207], v[182:183] neg_lo:[0,0,1] neg_hi:[0,0,1]
	v_pk_mul_f32 v[218:219], v[54:55], v[218:219]
	v_pk_mul_f32 v[216:217], v[40:41], v[216:217]
	v_pk_fma_f32 v[206:207], v[46:47], v[206:207], v[214:215]
	v_pk_fma_f32 v[176:177], v[56:57], v[212:213], v[176:177] neg_lo:[0,0,1] neg_hi:[0,0,1]
	v_pk_mul_f32 v[178:179], v[152:153], v[178:179] op_sel_hi:[0,1]
	v_pk_fma_f32 v[180:181], v[40:41], v[208:209], v[180:181] neg_lo:[0,0,1] neg_hi:[0,0,1]
	v_pk_mul_f32 v[220:221], v[56:57], v[220:221]
	v_pk_fma_f32 v[210:211], v[62:63], v[210:211], v[218:219]
	v_pk_fma_f32 v[208:209], v[48:49], v[208:209], v[216:217]
	v_pk_mul_f32 v[216:217], v[152:153], v[206:207] op_sel_hi:[0,1]
	v_cvt_pk_bf16_f32 v206, v178, v179
	v_pk_mul_f32 v[176:177], v[152:153], v[176:177] op_sel_hi:[0,1]
	v_pk_mul_f32 v[180:181], v[152:153], v[180:181] op_sel_hi:[0,1]
	v_pk_mul_f32 v[182:183], v[152:153], v[182:183] op_sel_hi:[0,1]
	v_pk_fma_f32 v[212:213], v[64:65], v[212:213], v[220:221]
	v_pk_mul_f32 v[210:211], v[152:153], v[210:211] op_sel_hi:[0,1]
	v_pk_mul_f32 v[214:215], v[152:153], v[208:209] op_sel_hi:[0,1]
	v_cvt_pk_bf16_f32 v207, v176, v177
	v_cvt_pk_bf16_f32 v208, v182, v183
	v_cvt_pk_bf16_f32 v209, v180, v181
	global_store_dwordx4 v[164:165], v[206:209], off
	v_pk_mul_f32 v[212:213], v[152:153], v[212:213] op_sel_hi:[0,1]
	s_nop 0
	v_cvt_pk_bf16_f32 v206, v210, v211
	v_cvt_pk_bf16_f32 v207, v212, v213
	v_cvt_pk_bf16_f32 v208, v216, v217
	v_cvt_pk_bf16_f32 v209, v214, v215
	global_store_dwordx4 v[164:165], v[206:209], off offset:256
	s_nop 1
	v_lshl_add_u64 v[164:165], v[164:165], 0, s[8:9]
	s_waitcnt vmcnt(14)
; __device__ __forceinline__ unsigned cvt_pk_bf16(float lo, float hi) { unsigned r; asm volatile("v_cvt_pk_bf16_f32 %0, %1, %2" : "=v"(r) : "v"(lo), "v"(hi)); return r; }
;     __device__ __forceinline__ void operator()(const f32x4 (&acc)[2][2][4][2], const Unit& u, int wr, int wc, int fr, int fq) const {
;     ...
;                 for (int m = 0; m < 4; ++m) { const int row = row0 + ai * HALF + m * 16; bf16_t* rowp = O + (size_t)row * ldc + col0;
;                     const f32x4 c0 = *(const f32x4*)(ct + (size_t)row * 128 + j0), c1 = *(const f32x4*)(ct + (size_t)row * 128 + j0 + 4);
;                     const f32x4 s0 = *(const f32x4*)(st + (size_t)row * 128 + j0), s1 = *(const f32x4*)(st + (size_t)row * 128 + j0 + 4);
;                     const f32x4 a0 = acc[ai][0][m][0], a1 = acc[ai][0][m][1], b0 = acc[ai][1][m][0], b1 = acc[ai][1][m][1];
;                     const f32x4 p0 = (a0 * c0 - b0 * s0) * sc, p1 = (a1 * c1 - b1 * s1) * sc, q0 = (a0 * s0 + b0 * c0) * sc, q1 = (a1 * s1 + b1 * c1) * sc;
;                     u32x4 w; w.x = cvt_pk_bf16(p0[0], p0[1]); w.y = cvt_pk_bf16(p0[2], p0[3]); w.z = cvt_pk_bf16(p1[0], p1[1]); w.w = cvt_pk_bf16(p1[2], p1[3]);
;                     *(u32x4*)rowp = w;
;                     w.x = cvt_pk_bf16(q0[0], q0[1]); w.y = cvt_pk_bf16(q0[2], q0[3]); w.z = cvt_pk_bf16(q1[0], q1[1]); w.w = cvt_pk_bf16(q1[2], q1[3]);
;                     *(u32x4*)(rowp + HALF) = w; }
	v_pk_mul_f32 v[182:183], v[42:43], v[114:115]
	v_pk_mul_f32 v[178:179], v[58:59], v[122:123]
	v_pk_mul_f32 v[114:115], v[34:35], v[114:115]
	v_pk_mul_f32 v[176:177], v[60:61], v[124:125]
	v_pk_fma_f32 v[178:179], v[50:51], v[106:107], v[178:179] neg_lo:[0,0,1] neg_hi:[0,0,1]
	v_pk_mul_f32 v[180:181], v[44:45], v[116:117]
	v_pk_fma_f32 v[182:183], v[34:35], v[98:99], v[182:183] neg_lo:[0,0,1] neg_hi:[0,0,1]
	v_pk_mul_f32 v[122:123], v[50:51], v[122:123]
	v_pk_mul_f32 v[116:117], v[36:37], v[116:117]
	v_pk_fma_f32 v[98:99], v[42:43], v[98:99], v[114:115]
	v_pk_fma_f32 v[176:177], v[52:53], v[108:109], v[176:177] neg_lo:[0,0,1] neg_hi:[0,0,1]
	v_pk_mul_f32 v[178:179], v[152:153], v[178:179] op_sel_hi:[0,1]
	v_pk_fma_f32 v[180:181], v[36:37], v[100:101], v[180:181] neg_lo:[0,0,1] neg_hi:[0,0,1]
	v_pk_mul_f32 v[124:125], v[52:53], v[124:125]
	v_pk_fma_f32 v[106:107], v[58:59], v[106:107], v[122:123]
	v_pk_fma_f32 v[100:101], v[44:45], v[100:101], v[116:117]
	v_pk_mul_f32 v[116:117], v[152:153], v[98:99] op_sel_hi:[0,1]
	v_cvt_pk_bf16_f32 v98, v178, v179
	v_pk_mul_f32 v[176:177], v[152:153], v[176:177] op_sel_hi:[0,1]
	v_pk_mul_f32 v[180:181], v[152:153], v[180:181] op_sel_hi:[0,1]
	v_pk_mul_f32 v[182:183], v[152:153], v[182:183] op_sel_hi:[0,1]
	v_pk_fma_f32 v[108:109], v[60:61], v[108:109], v[124:125]
	v_pk_mul_f32 v[106:107], v[152:153], v[106:107] op_sel_hi:[0,1]
	v_pk_mul_f32 v[114:115], v[152:153], v[100:101] op_sel_hi:[0,1]
	v_cvt_pk_bf16_f32 v99, v176, v177
	v_cvt_pk_bf16_f32 v100, v182, v183
	v_cvt_pk_bf16_f32 v101, v180, v181
	global_store_dwordx4 v[164:165], v[98:101], off
	v_pk_mul_f32 v[108:109], v[152:153], v[108:109] op_sel_hi:[0,1]
	s_nop 0
	v_cvt_pk_bf16_f32 v98, v106, v107
	v_cvt_pk_bf16_f32 v99, v108, v109
	v_cvt_pk_bf16_f32 v100, v116, v117
	v_cvt_pk_bf16_f32 v101, v114, v115
	global_store_dwordx4 v[164:165], v[98:101], off offset:256
	s_nop 1
	v_lshl_add_u64 v[164:165], v[164:165], 0, s[8:9]
	s_waitcnt vmcnt(10)
	v_pk_mul_f32 v[182:183], v[14:15], v[118:119]
	v_pk_mul_f32 v[178:179], v[30:31], v[126:127]
	v_pk_mul_f32 v[118:119], v[6:7], v[118:119]
	v_pk_mul_f32 v[176:177], v[32:33], v[128:129]
	v_pk_fma_f32 v[178:179], v[22:23], v[110:111], v[178:179] neg_lo:[0,0,1] neg_hi:[0,0,1]
	v_pk_mul_f32 v[180:181], v[16:17], v[120:121]
	v_pk_fma_f32 v[182:183], v[6:7], v[102:103], v[182:183] neg_lo:[0,0,1] neg_hi:[0,0,1]
	v_pk_mul_f32 v[126:127], v[22:23], v[126:127]
	v_pk_mul_f32 v[120:121], v[8:9], v[120:121]
	v_pk_fma_f32 v[102:103], v[14:15], v[102:103], v[118:119]
	v_pk_fma_f32 v[176:177], v[24:25], v[112:113], v[176:177] neg_lo:[0,0,1] neg_hi:[0,0,1]
	v_pk_mul_f32 v[178:179], v[152:153], v[178:179] op_sel_hi:[0,1]
	v_pk_fma_f32 v[180:181], v[8:9], v[104:105], v[180:181] neg_lo:[0,0,1] neg_hi:[0,0,1]
	v_pk_mul_f32 v[128:129], v[24:25], v[128:129]
	v_pk_fma_f32 v[110:111], v[30:31], v[110:111], v[126:127]
	v_pk_fma_f32 v[104:105], v[16:17], v[104:105], v[120:121]
	v_pk_mul_f32 v[120:121], v[152:153], v[102:103] op_sel_hi:[0,1]
	v_cvt_pk_bf16_f32 v102, v178, v179
	v_pk_mul_f32 v[176:177], v[152:153], v[176:177] op_sel_hi:[0,1]
	v_pk_mul_f32 v[180:181], v[152:153], v[180:181] op_sel_hi:[0,1]
	v_pk_mul_f32 v[182:183], v[152:153], v[182:183] op_sel_hi:[0,1]
	v_pk_fma_f32 v[112:113], v[32:33], v[112:113], v[128:129]
	v_pk_mul_f32 v[110:111], v[152:153], v[110:111] op_sel_hi:[0,1]
	v_pk_mul_f32 v[118:119], v[152:153], v[104:105] op_sel_hi:[0,1]
	v_cvt_pk_bf16_f32 v103, v176, v177
	v_cvt_pk_bf16_f32 v104, v182, v183
	v_cvt_pk_bf16_f32 v105, v180, v181
	global_store_dwordx4 v[164:165], v[102:105], off
	v_pk_mul_f32 v[112:113], v[152:153], v[112:113] op_sel_hi:[0,1]
	s_nop 0
	v_cvt_pk_bf16_f32 v102, v110, v111
	v_cvt_pk_bf16_f32 v103, v112, v113
	v_cvt_pk_bf16_f32 v104, v120, v121
	v_cvt_pk_bf16_f32 v105, v118, v119
	global_store_dwordx4 v[164:165], v[102:105], off offset:256
	s_nop 1
	v_lshl_add_u64 v[164:165], v[164:165], 0, s[8:9]
	s_waitcnt vmcnt(6)
	v_pk_mul_f32 v[180:181], v[12:13], v[140:141]
	v_pk_mul_f32 v[176:177], v[28:29], v[174:175]
	v_pk_mul_f32 v[178:179], v[26:27], v[172:173]
	v_pk_mul_f32 v[182:183], v[10:11], v[138:139]
	v_pk_mul_f32 v[140:141], v[4:5], v[140:141]
	v_pk_mul_f32 v[138:139], v[2:3], v[138:139]
	v_pk_fma_f32 v[176:177], v[20:21], v[136:137], v[176:177] neg_lo:[0,0,1] neg_hi:[0,0,1]
	v_pk_fma_f32 v[178:179], v[18:19], v[134:135], v[178:179] neg_lo:[0,0,1] neg_hi:[0,0,1]
	v_pk_fma_f32 v[180:181], v[4:5], v[132:133], v[180:181] neg_lo:[0,0,1] neg_hi:[0,0,1]
	v_pk_fma_f32 v[182:183], v[2:3], v[130:131], v[182:183] neg_lo:[0,0,1] neg_hi:[0,0,1]
	v_pk_mul_f32 v[174:175], v[20:21], v[174:175]
	v_pk_mul_f32 v[172:173], v[18:19], v[172:173]
	v_pk_fma_f32 v[132:133], v[12:13], v[132:133], v[140:141]
	v_pk_fma_f32 v[130:131], v[10:11], v[130:131], v[138:139]
	v_pk_mul_f32 v[176:177], v[152:153], v[176:177] op_sel_hi:[0,1]
	v_pk_mul_f32 v[178:179], v[152:153], v[178:179] op_sel_hi:[0,1]
	v_pk_mul_f32 v[180:181], v[152:153], v[180:181] op_sel_hi:[0,1]
	v_pk_mul_f32 v[182:183], v[152:153], v[182:183] op_sel_hi:[0,1]
	v_pk_fma_f32 v[136:137], v[28:29], v[136:137], v[174:175]
	v_pk_fma_f32 v[134:135], v[26:27], v[134:135], v[172:173]
	v_pk_mul_f32 v[138:139], v[152:153], v[132:133] op_sel_hi:[0,1]
	v_pk_mul_f32 v[140:141], v[152:153], v[130:131] op_sel_hi:[0,1]
	v_cvt_pk_bf16_f32 v130, v178, v179
	v_cvt_pk_bf16_f32 v131, v176, v177
	v_cvt_pk_bf16_f32 v132, v182, v183
	v_cvt_pk_bf16_f32 v133, v180, v181
	v_pk_mul_f32 v[136:137], v[152:153], v[136:137] op_sel_hi:[0,1]
	v_pk_mul_f32 v[134:135], v[152:153], v[134:135] op_sel_hi:[0,1]
	global_store_dwordx4 v[164:165], v[130:133], off
	s_nop 1
	v_cvt_pk_bf16_f32 v130, v134, v135
	v_cvt_pk_bf16_f32 v131, v136, v137
	v_cvt_pk_bf16_f32 v132, v140, v141
	v_cvt_pk_bf16_f32 v133, v138, v139
	global_store_dwordx4 v[164:165], v[130:133], off offset:256
